# baseline (speedup 1.0000x reference)
.Lg0_cloop:
	s_mul_i32 s8, s3, 0x7000
	s_barrier
	v_add_u32_e32 v103, s8, v100
	v_add_u32_e32 v101, s8, v99
	ds_read_b128 v[146:149], v103 offset:12288
	ds_read_b128 v[150:153], v103 offset:13312
	ds_read_b128 v[154:157], v103 offset:14336
	ds_read_b128 v[158:161], v103 offset:15360
	s_waitcnt lgkmcnt(9)
	v_mfma_f32_16x16x32_f16 v[94:97], v[122:125], v[104:107], v[94:97]
	s_add_i32 s8, s3, 1
	s_cmp_lg_u32 s3, 4
	s_cselect_b32 s3, s8, 0
	v_mfma_f32_16x16x32_f16 v[70:73], v[122:125], v[108:111], v[70:73]
	v_mfma_f32_16x16x32_f16 v[46:49], v[122:125], v[112:115], v[46:49]
	v_mfma_f32_16x16x32_f16 v[22:25], v[122:125], v[116:119], v[22:25]
	ds_read_b128 v[122:125], v101
	s_waitcnt lgkmcnt(9)
	v_mfma_f32_16x16x32_f16 v[90:93], v[126:129], v[104:107], v[90:93]
	v_mfma_f32_16x16x32_f16 v[66:69], v[126:129], v[108:111], v[66:69]
	v_mfma_f32_16x16x32_f16 v[42:45], v[126:129], v[112:115], v[42:45]
	v_mfma_f32_16x16x32_f16 v[18:21], v[126:129], v[116:119], v[18:21]
	ds_read_b128 v[126:129], v101 offset:1024
	s_waitcnt lgkmcnt(9)
	v_mfma_f32_16x16x32_f16 v[86:89], v[130:133], v[104:107], v[86:89]
	v_mfma_f32_16x16x32_f16 v[54:57], v[130:133], v[108:111], v[54:57]
	v_mfma_f32_16x16x32_f16 v[26:29], v[130:133], v[112:115], v[26:29]
	v_mfma_f32_16x16x32_f16 v[6:9], v[130:133], v[116:119], v[6:9]
	ds_read_b128 v[130:133], v101 offset:2048
	s_waitcnt lgkmcnt(9)
	v_mfma_f32_16x16x32_f16 v[74:77], v[134:137], v[104:107], v[74:77]
	v_mfma_f32_16x16x32_f16 v[50:53], v[134:137], v[108:111], v[50:53]
	v_mfma_f32_16x16x32_f16 v[38:41], v[134:137], v[112:115], v[38:41]
	v_mfma_f32_16x16x32_f16 v[14:17], v[134:137], v[116:119], v[14:17]
	ds_read_b128 v[134:137], v101 offset:3072
	s_waitcnt lgkmcnt(9)
	v_mfma_f32_16x16x32_f16 v[82:85], v[138:141], v[104:107], v[82:85]
	v_mfma_f32_16x16x32_f16 v[58:61], v[138:141], v[108:111], v[58:61]
	v_mfma_f32_16x16x32_f16 v[30:33], v[138:141], v[112:115], v[30:33]
	v_mfma_f32_16x16x32_f16 v[10:13], v[138:141], v[116:119], v[10:13]
	ds_read_b128 v[138:141], v101 offset:4096
	s_waitcnt lgkmcnt(9)
	v_mfma_f32_16x16x32_f16 v[78:81], v[142:145], v[104:107], v[78:81]
	v_mfma_f32_16x16x32_f16 v[62:65], v[142:145], v[108:111], v[62:65]
	v_mfma_f32_16x16x32_f16 v[34:37], v[142:145], v[112:115], v[34:37]
	v_mfma_f32_16x16x32_f16 v[2:5], v[142:145], v[116:119], v[2:5]
	ds_read_b128 v[142:145], v101 offset:5120
	s_mul_i32 s8, s3, 0x7000
	s_barrier
	v_add_u32_e32 v103, s8, v100
	v_add_u32_e32 v101, s8, v99
	ds_read_b128 v[104:107], v103 offset:12288
	ds_read_b128 v[108:111], v103 offset:13312
	ds_read_b128 v[112:115], v103 offset:14336
	ds_read_b128 v[116:119], v103 offset:15360
	s_waitcnt lgkmcnt(9)
	v_mfma_f32_16x16x32_f16 v[94:97], v[122:125], v[146:149], v[94:97]
	s_add_i32 s8, s3, 1
	s_cmp_lg_u32 s3, 4
	s_cselect_b32 s3, s8, 0
	v_mfma_f32_16x16x32_f16 v[70:73], v[122:125], v[150:153], v[70:73]
	v_mfma_f32_16x16x32_f16 v[46:49], v[122:125], v[154:157], v[46:49]
	v_mfma_f32_16x16x32_f16 v[22:25], v[122:125], v[158:161], v[22:25]
	ds_read_b128 v[122:125], v101
	s_waitcnt lgkmcnt(9)
	v_mfma_f32_16x16x32_f16 v[90:93], v[126:129], v[146:149], v[90:93]
	v_mfma_f32_16x16x32_f16 v[66:69], v[126:129], v[150:153], v[66:69]
	v_mfma_f32_16x16x32_f16 v[42:45], v[126:129], v[154:157], v[42:45]
	v_mfma_f32_16x16x32_f16 v[18:21], v[126:129], v[158:161], v[18:21]
	ds_read_b128 v[126:129], v101 offset:1024
	s_waitcnt lgkmcnt(9)
	v_mfma_f32_16x16x32_f16 v[86:89], v[130:133], v[146:149], v[86:89]
	v_mfma_f32_16x16x32_f16 v[54:57], v[130:133], v[150:153], v[54:57]
	v_mfma_f32_16x16x32_f16 v[26:29], v[130:133], v[154:157], v[26:29]
	v_mfma_f32_16x16x32_f16 v[6:9], v[130:133], v[158:161], v[6:9]
	ds_read_b128 v[130:133], v101 offset:2048
	s_waitcnt lgkmcnt(9)
	v_mfma_f32_16x16x32_f16 v[74:77], v[134:137], v[146:149], v[74:77]
	v_mfma_f32_16x16x32_f16 v[50:53], v[134:137], v[150:153], v[50:53]
	v_mfma_f32_16x16x32_f16 v[38:41], v[134:137], v[154:157], v[38:41]
	v_mfma_f32_16x16x32_f16 v[14:17], v[134:137], v[158:161], v[14:17]
	ds_read_b128 v[134:137], v101 offset:3072
	s_waitcnt lgkmcnt(9)
	v_mfma_f32_16x16x32_f16 v[82:85], v[138:141], v[146:149], v[82:85]
	v_mfma_f32_16x16x32_f16 v[58:61], v[138:141], v[150:153], v[58:61]
	v_mfma_f32_16x16x32_f16 v[30:33], v[138:141], v[154:157], v[30:33]
	v_mfma_f32_16x16x32_f16 v[10:13], v[138:141], v[158:161], v[10:13]
	ds_read_b128 v[138:141], v101 offset:4096
	s_waitcnt lgkmcnt(9)
	v_mfma_f32_16x16x32_f16 v[78:81], v[142:145], v[146:149], v[78:81]
	v_mfma_f32_16x16x32_f16 v[62:65], v[142:145], v[150:153], v[62:65]
	v_mfma_f32_16x16x32_f16 v[34:37], v[142:145], v[154:157], v[34:37]
	v_mfma_f32_16x16x32_f16 v[2:5], v[142:145], v[158:161], v[2:5]
	ds_read_b128 v[142:145], v101 offset:5120
	s_add_i32 s7, s7, -1
	s_cmp_eq_u32 s7, 0
	s_cbranch_scc0 .Lg0_cloop
	s_waitcnt lgkmcnt(0)
	s_barrier
	s_mul_i32 s24, s22, 0x3400
	s_lshl_b32 s28, s2, 6
	s_add_i32 s29, s20, s28
	s_and_b32 s30, s29, 0x7ff
	v_add_u32_e32 v98, s30, v102
	v_lshlrev_b32_e32 v98, 8, v98
	v_lshl_add_u32 v98, v120, 4, v98
	v_add_u32_e32 v99, 0x1000, v98
	v_add_u32_e32 v100, 0x2000, v98
	v_add_u32_e32 v101, 0x3000, v98
	v_mul_u32_u24_e32 v103, 0xd0, v102
	v_lshl_add_u32 v103, v120, 3, v103
	v_add_u32_e32 v103, s24, v103
	v_lshrrev_b32_e32 v0, 2, v1
	v_and_b32_e32 v1, 3, v1
	v_mul_u32_u24_e32 v102, 0xd0, v0
	v_lshl_add_u32 v102, v1, 4, v102
	v_add_u32_e32 v102, s24, v102
	v_lshlrev_b32_e32 v0, 11, v0
	v_lshl_add_u32 v0, v1, 4, v0
	s_lshl_b32 s31, s5, 7
	s_add_i32 s35, s31, 0
	s_and_b32 s35, s35, 0xff
	s_add_u32 s36, s12, s35
	s_addc_u32 s37, s13, 0
	s_add_i32 s35, s31, 64
	s_and_b32 s35, s35, 0xff
	s_add_u32 s38, s12, s35
	s_addc_u32 s39, s13, 0
	s_add_i32 s35, s31, 128
	s_and_b32 s35, s35, 0xff
	s_add_u32 s40, s12, s35
	s_addc_u32 s41, s13, 0
	s_add_i32 s35, s31, 192
	s_and_b32 s35, s35, 0xff
	s_add_u32 s42, s12, s35
	s_addc_u32 s43, s13, 0
	s_add_i32 s34, s25, s23
	s_sub_i32 s32, 0x400, s34
	s_ashr_i32 s32, s32, 4
	s_max_i32 s32, s32, 0
	s_min_i32 s32, s32, 6
	s_sub_i32 s33, 0x800, s34
	s_ashr_i32 s33, s33, 4
	s_max_i32 s33, s33, 0
	s_min_i32 s33, s33, 6
	s_cmp_ge_u32 s23, 0x800
	s_cbranch_scc1 .Lepi_noload
	s_cmp_lg_u32 s5, 0
	s_cbranch_scc1 .Lepi_ld1
	global_load_dwordx4 v[104:107], v98, s[36:37]
	global_load_dwordx4 v[108:111], v98, s[38:39]
	global_load_dwordx4 v[112:115], v98, s[40:41]
	global_load_dwordx4 v[116:119], v98, s[42:43]
	global_load_dwordx4 v[120:123], v99, s[36:37]
	global_load_dwordx4 v[124:127], v99, s[38:39]
	global_load_dwordx4 v[128:131], v99, s[40:41]
	global_load_dwordx4 v[132:135], v99, s[42:43]
	s_lshl_b32 s35, s2, 14
	s_waitcnt vmcnt(0)
	v_mbcnt_lo_u32_b32 v98, -1, 0
	v_mbcnt_hi_u32_b32 v98, -1, v98
	v_lshlrev_b32_e32 v98, 4, v98
	v_add_u32_e32 v98, s35, v98
	ds_write_b128 v98, v[104:107] offset:0
	ds_write_b128 v98, v[108:111] offset:1024
	ds_write_b128 v98, v[112:115] offset:2048
	ds_write_b128 v98, v[116:119] offset:3072
	ds_write_b128 v98, v[120:123] offset:4096
	ds_write_b128 v98, v[124:127] offset:5120
	ds_write_b128 v98, v[128:131] offset:6144
	ds_write_b128 v98, v[132:135] offset:7168
	s_waitcnt lgkmcnt(0)
	s_barrier
	ds_read_b128 v[136:139], v98 offset:8192
	ds_read_b128 v[140:143], v98 offset:9216
	ds_read_b128 v[144:147], v98 offset:10240
	ds_read_b128 v[148:151], v98 offset:11264
	ds_read_b128 v[152:155], v98 offset:12288
	ds_read_b128 v[156:159], v98 offset:13312
	ds_read_b128 v[160:163], v98 offset:14336
	ds_read_b128 v[164:167], v98 offset:15360
	s_waitcnt lgkmcnt(0)
	s_barrier
	s_branch .Lepi_noload
.Lepi_ld1:
	global_load_dwordx4 v[136:139], v100, s[36:37]
	global_load_dwordx4 v[140:143], v100, s[38:39]
	global_load_dwordx4 v[144:147], v100, s[40:41]
	global_load_dwordx4 v[148:151], v100, s[42:43]
	global_load_dwordx4 v[152:155], v101, s[36:37]
	global_load_dwordx4 v[156:159], v101, s[38:39]
	global_load_dwordx4 v[160:163], v101, s[40:41]
	global_load_dwordx4 v[164:167], v101, s[42:43]
	s_lshl_b32 s35, s2, 14
	s_waitcnt vmcnt(0)
	v_mbcnt_lo_u32_b32 v98, -1, 0
	v_mbcnt_hi_u32_b32 v98, -1, v98
	v_lshlrev_b32_e32 v98, 4, v98
	v_add_u32_e32 v98, s35, v98
	ds_write_b128 v98, v[136:139] offset:10240
	ds_write_b128 v98, v[140:143] offset:11264
	ds_write_b128 v98, v[144:147] offset:8192
	ds_write_b128 v98, v[148:151] offset:9216
	ds_write_b128 v98, v[152:155] offset:14336
	ds_write_b128 v98, v[156:159] offset:15360
	ds_write_b128 v98, v[160:163] offset:12288
	ds_write_b128 v98, v[164:167] offset:13312
	s_waitcnt lgkmcnt(0)
	s_barrier
	ds_read_b128 v[104:107], v98 offset:2048
	ds_read_b128 v[108:111], v98 offset:3072
	ds_read_b128 v[112:115], v98 offset:0
	ds_read_b128 v[116:119], v98 offset:1024
	ds_read_b128 v[120:123], v98 offset:6144
	ds_read_b128 v[124:127], v98 offset:7168
	ds_read_b128 v[128:131], v98 offset:4096
	ds_read_b128 v[132:135], v98 offset:5120
	s_waitcnt lgkmcnt(0)
	s_barrier
